# P10 epilogue Y stores marked nt (streaming output read once by the combine phase)
# speedup vs baseline: 1.0012x; 1.0012x over previous
; #define LAS __attribute__((address_space(3)))
; __device__ __forceinline__ unsigned pk4_fp8(float a, float b, float c, float d) { int w = 0; w = __builtin_amdgcn_cvt_pk_fp8_f32(a, b, w, false); w = __builtin_amdgcn_cvt_pk_fp8_f32(c, d, w, true); return (unsigned)w; }
;     __device__ __forceinline__ void operator()(const Acc& acc, const Unit& u, int wr, int wc, int fr, int fq) const { if (u.e == 0) rs(acc, u, wr, wc, fr, fq); else cs(acc, u, wr, wc, fr, fq); }
;     __device__ __forceinline__ void operator()(const Acc& acc, const Unit& u, int wr, int wc, int fr, int fq) const {
;         const int col0 = u.pn * 256 + wc * 32 + 8 * fq; const LAS float* bl = slots + (u.idx & 1) * 512 + 256 + wc * 32 + 8 * fq;
;         f32x4 bb[2][2];
; #pragma unroll
;         for (int bj = 0; bj < 2; ++bj) { bb[bj][0] = *(const LAS f32x4*)(bl + bj * 128); bb[bj][1] = *(const LAS f32x4*)(bl + bj * 128 + 4); }
; #pragma unroll
;         for (int bj = 0; bj < 2; ++bj) { const f32x4 b0 = bb[bj][0], b1 = bb[bj][1];
; #pragma unroll
;             for (int ai = 0; ai < 2; ++ai)
; #pragma unroll
;                 for (int m = 0; m < 4; ++m) { const f32x4 v0 = acc[ai][bj][m][0] + b0, v1 = acc[ai][bj][m][1] + b1; v2u w; w.x = pk4_fp8(v0[0], v0[1], v0[2], v0[3]); w.y = pk4_fp8(v1[0], v1[1], v1[2], v1[3]);
;                     *(v2u*)(y + (size_t)EPI_ROWS(ai, m) * DM + col0 + bj * 128) = w; } }
.LBB5_1681:
	s_lshl_b32 s18, s57, 11
	s_and_b32 s18, s18, 0x800
	v_mov_b32_e32 v138, v143
	v_mov_b32_e32 v151, v144
	s_add_i32 s18, s49, s18
	s_lshl_b32 vcc_lo, s46, 2
	s_add_i32 s18, s18, vcc_lo
	v_mov_b32_e32 v162, v139
	v_lshl_add_u32 v134, v151, 6, s18
	ds_read_b128 v[152:155], v134 offset:1024
	ds_read_b128 v[156:159], v134 offset:1040
	ds_read_b128 v[130:133], v134 offset:1056
	ds_read_b128 v[134:137], v134 offset:1072
	v_mov_b32_e32 v163, v139
	s_waitcnt lgkmcnt(0)
	v_pk_add_f32 v[126:127], v[126:127], v[152:153]
	v_pk_add_f32 v[114:115], v[114:115], v[156:157]
	v_cvt_pk_fp8_f32 v162, v126, v127
	v_mov_b32_e32 v127, v139
	v_cvt_pk_fp8_f32 v127, v114, v115
	v_pk_add_f32 v[116:117], v[116:117], v[158:159]
	v_pk_add_f32 v[106:107], v[106:107], v[156:157]
	v_pk_add_f32 v[108:109], v[108:109], v[158:159]
	v_cvt_pk_fp8_f32 v127, v116, v117 op_sel:[0,0,1]
	v_mov_b32_e32 v117, v139
	v_cvt_pk_fp8_f32 v117, v106, v107
	v_pk_add_f32 v[98:99], v[98:99], v[156:157]
	v_pk_add_f32 v[100:101], v[100:101], v[158:159]
	v_pk_add_f32 v[90:91], v[90:91], v[156:157]
	v_cvt_pk_fp8_f32 v117, v108, v109 op_sel:[0,0,1]
	v_mov_b32_e32 v109, v139
	v_cvt_pk_fp8_f32 v109, v98, v99
	v_pk_add_f32 v[92:93], v[92:93], v[158:159]
	v_pk_add_f32 v[82:83], v[82:83], v[156:157]
	v_pk_add_f32 v[84:85], v[84:85], v[158:159]
	v_cvt_pk_fp8_f32 v109, v100, v101 op_sel:[0,0,1]
	v_mov_b32_e32 v101, v139
	v_cvt_pk_fp8_f32 v101, v90, v91
	v_pk_add_f32 v[74:75], v[74:75], v[156:157]
	v_pk_add_f32 v[76:77], v[76:77], v[158:159]
	v_pk_add_f32 v[58:59], v[58:59], v[156:157]
	v_cvt_pk_fp8_f32 v101, v92, v93 op_sel:[0,0,1]
	v_mov_b32_e32 v93, v139
	v_cvt_pk_fp8_f32 v93, v82, v83
	v_pk_add_f32 v[60:61], v[60:61], v[158:159]
	v_pk_add_f32 v[54:55], v[54:55], v[130:131]
	v_pk_add_f32 v[50:51], v[50:51], v[134:135]
	v_cvt_pk_fp8_f32 v93, v84, v85 op_sel:[0,0,1]
	v_mov_b32_e32 v85, v139
	v_cvt_pk_fp8_f32 v85, v74, v75
	v_pk_add_f32 v[46:47], v[46:47], v[130:131]
	v_pk_add_f32 v[42:43], v[42:43], v[134:135]
	v_pk_add_f32 v[38:39], v[38:39], v[130:131]
	v_cvt_pk_fp8_f32 v85, v76, v77 op_sel:[0,0,1]
	v_mov_b32_e32 v77, v139
	v_cvt_pk_fp8_f32 v77, v58, v59
	v_pk_add_f32 v[58:59], v[64:65], v[154:155]
	v_mov_b32_e32 v64, v139
	v_pk_add_f32 v[34:35], v[34:35], v[134:135]
	v_cvt_pk_fp8_f32 v77, v60, v61 op_sel:[0,0,1]
	v_pk_add_f32 v[60:61], v[70:71], v[130:131]
	v_pk_add_f32 v[30:31], v[30:31], v[130:131]
	v_cvt_pk_fp8_f32 v64, v60, v61
	v_pk_add_f32 v[60:61], v[72:73], v[132:133]
	v_pk_add_f32 v[26:27], v[26:27], v[134:135]
	v_pk_add_f32 v[22:23], v[22:23], v[130:131]
	v_cvt_pk_fp8_f32 v64, v60, v61 op_sel:[0,0,1]
	v_mov_b32_e32 v60, v139
	v_cvt_pk_fp8_f32 v60, v54, v55
	v_mov_b32_e32 v61, v139
	v_cvt_pk_fp8_f32 v61, v50, v51
	v_pk_add_f32 v[50:51], v[56:57], v[132:133]
	v_pk_add_f32 v[18:19], v[18:19], v[134:135]
	v_cvt_pk_fp8_f32 v60, v50, v51 op_sel:[0,0,1]
	v_mov_b32_e32 v50, v139
	v_cvt_pk_fp8_f32 v50, v46, v47
	v_mov_b32_e32 v51, v139
	v_cvt_pk_fp8_f32 v51, v42, v43
	v_pk_add_f32 v[42:43], v[48:49], v[132:133]
	v_pk_add_f32 v[122:123], v[122:123], v[156:157]
	v_cvt_pk_fp8_f32 v50, v42, v43 op_sel:[0,0,1]
	v_mov_b32_e32 v42, v139
	v_cvt_pk_fp8_f32 v42, v38, v39
	v_mov_b32_e32 v43, v139
	v_cvt_pk_fp8_f32 v43, v34, v35
	v_pk_add_f32 v[34:35], v[40:41], v[132:133]
	v_pk_add_f32 v[14:15], v[14:15], v[130:131]
	v_cvt_pk_fp8_f32 v42, v34, v35 op_sel:[0,0,1]
	v_mov_b32_e32 v34, v139
	v_cvt_pk_fp8_f32 v34, v30, v31
	v_mov_b32_e32 v35, v139
	v_cvt_pk_fp8_f32 v35, v26, v27
	v_pk_add_f32 v[26:27], v[32:33], v[132:133]
	v_cvt_pk_fp8_f32 v163, v122, v123
	v_cvt_pk_fp8_f32 v34, v26, v27 op_sel:[0,0,1]
	v_mov_b32_e32 v26, v139
	v_cvt_pk_fp8_f32 v26, v22, v23
	v_mov_b32_e32 v27, v139
	v_cvt_pk_fp8_f32 v27, v18, v19
	v_pk_add_f32 v[18:19], v[24:25], v[132:133]
	v_pk_add_f32 v[118:119], v[118:119], v[152:153]
	v_cvt_pk_fp8_f32 v26, v18, v19 op_sel:[0,0,1]
	v_mov_b32_e32 v18, v139
	v_mov_b32_e32 v126, v139
	v_pk_add_f32 v[110:111], v[110:111], v[152:153]
	v_mov_b32_e32 v116, v139
	v_pk_add_f32 v[102:103], v[102:103], v[152:153]
	v_mov_b32_e32 v108, v139
	v_pk_add_f32 v[94:95], v[94:95], v[152:153]
	v_mov_b32_e32 v100, v139
	v_pk_add_f32 v[86:87], v[86:87], v[152:153]
	v_mov_b32_e32 v92, v139
	v_pk_add_f32 v[78:79], v[78:79], v[152:153]
	v_mov_b32_e32 v84, v139
	v_pk_add_f32 v[62:63], v[62:63], v[152:153]
	v_mov_b32_e32 v76, v139
	v_cvt_pk_fp8_f32 v18, v14, v15
	v_cvt_pk_fp8_f32 v126, v118, v119
	v_cvt_pk_fp8_f32 v116, v110, v111
	v_cvt_pk_fp8_f32 v108, v102, v103
	v_cvt_pk_fp8_f32 v100, v94, v95
	v_cvt_pk_fp8_f32 v92, v86, v87
	v_cvt_pk_fp8_f32 v84, v78, v79
	v_cvt_pk_fp8_f32 v76, v62, v63
	v_pk_add_f32 v[62:63], v[66:67], v[134:135]
	v_mov_b32_e32 v65, v139
	s_lshl_b32 s11, s11, 8
	v_cvt_pk_fp8_f32 v65, v62, v63
	v_pk_add_f32 v[10:11], v[10:11], v[134:135]
	v_mov_b32_e32 v19, v139
	v_pk_add_f32 v[124:125], v[124:125], v[158:159]
	s_add_i32 s11, s11, s45
	v_cvt_pk_fp8_f32 v19, v10, v11
	v_pk_add_f32 v[10:11], v[16:17], v[132:133]
	v_cvt_pk_fp8_f32 v163, v124, v125 op_sel:[0,0,1]
	v_add_u32_e32 v124, s11, v138
	v_pk_add_f32 v[114:115], v[120:121], v[154:155]
	v_pk_add_f32 v[106:107], v[112:113], v[154:155]
	v_pk_add_f32 v[98:99], v[104:105], v[154:155]
	v_pk_add_f32 v[90:91], v[96:97], v[154:155]
	v_pk_add_f32 v[82:83], v[88:89], v[154:155]
	v_pk_add_f32 v[74:75], v[80:81], v[154:155]
; #define LAS __attribute__((address_space(3)))
; __device__ __forceinline__ unsigned pk4_fp8(float a, float b, float c, float d) { int w = 0; w = __builtin_amdgcn_cvt_pk_fp8_f32(a, b, w, false); w = __builtin_amdgcn_cvt_pk_fp8_f32(c, d, w, true); return (unsigned)w; }
;     __device__ __forceinline__ void prefetch(const Unit& u) const { if (u.e == 0) rs.prefetch(u); else cs.prefetch(u); }
;     __device__ __forceinline__ void prefetch(const Unit& u) const { const int tid = threadIdx.x, w = __builtin_amdgcn_readfirstlane(tid >> 6);
;         if (w < 4) __builtin_amdgcn_global_load_lds((const unsigned*)(b_dn + (size_t)u.e * DM + u.pn * 256 + tid), (LAS unsigned*)(slots + (u.idx & 1) * 512 + 256 + w * 64), 4, 0, 0); }
;     __device__ __forceinline__ void operator()(const Acc& acc, const Unit& u, int wr, int wc, int fr, int fq) const {
;         const int col0 = u.pn * 256 + wc * 32 + 8 * fq; const LAS float* bl = slots + (u.idx & 1) * 512 + 256 + wc * 32 + 8 * fq;
;         f32x4 bb[2][2];
; #pragma unroll
;         for (int bj = 0; bj < 2; ++bj) { bb[bj][0] = *(const LAS f32x4*)(bl + bj * 128); bb[bj][1] = *(const LAS f32x4*)(bl + bj * 128 + 4); }
; #pragma unroll
;         for (int bj = 0; bj < 2; ++bj) { const f32x4 b0 = bb[bj][0], b1 = bb[bj][1];
; #pragma unroll
;             for (int ai = 0; ai < 2; ++ai)
; #pragma unroll
;                 for (int m = 0; m < 4; ++m) { const f32x4 v0 = acc[ai][bj][m][0] + b0, v1 = acc[ai][bj][m][1] + b1; v2u w; w.x = pk4_fp8(v0[0], v0[1], v0[2], v0[3]); w.y = pk4_fp8(v1[0], v1[1], v1[2], v1[3]);
;                     *(v2u*)(y + (size_t)EPI_ROWS(ai, m) * DM + col0 + bj * 128) = w; } }
	v_cvt_pk_fp8_f32 v18, v10, v11 op_sel:[0,0,1]
	v_pk_add_f32 v[6:7], v[6:7], v[130:131]
	v_pk_add_f32 v[2:3], v[2:3], v[134:135]
	v_mov_b32_e32 v10, v139
	v_mov_b32_e32 v11, v139
	s_lshl_b32 s18, s56, 8
	v_pk_add_f32 v[122:123], v[128:129], v[154:155]
	v_cvt_pk_fp8_f32 v126, v114, v115 op_sel:[0,0,1]
	v_add_u32_e32 v114, 16, v124
	v_cvt_pk_fp8_f32 v116, v106, v107 op_sel:[0,0,1]
	v_add_u32_e32 v106, 32, v124
	v_cvt_pk_fp8_f32 v108, v98, v99 op_sel:[0,0,1]
	v_add_u32_e32 v98, 48, v124
	v_cvt_pk_fp8_f32 v100, v90, v91 op_sel:[0,0,1]
	v_add_u32_e32 v90, 0x80, v124
	v_cvt_pk_fp8_f32 v92, v82, v83 op_sel:[0,0,1]
	v_add_u32_e32 v82, 0x90, v124
	v_cvt_pk_fp8_f32 v84, v74, v75 op_sel:[0,0,1]
	v_add_u32_e32 v74, 0xa0, v124
	v_cvt_pk_fp8_f32 v76, v58, v59 op_sel:[0,0,1]
	v_add_u32_e32 v58, 0xb0, v124
	v_pk_add_f32 v[62:63], v[68:69], v[136:137]
	v_pk_add_f32 v[28:29], v[28:29], v[136:137]
	v_cvt_pk_fp8_f32 v10, v6, v7
	v_cvt_pk_fp8_f32 v11, v2, v3
	s_add_i32 s18, s18, s46
	s_add_i32 s18, s18, s46
	v_cvt_pk_fp8_f32 v162, v122, v123 op_sel:[0,0,1]
	v_ashrrev_i32_e32 v125, 31, v124
	v_ashrrev_i32_e32 v115, 31, v114
	v_ashrrev_i32_e32 v107, 31, v106
	v_ashrrev_i32_e32 v99, 31, v98
	v_ashrrev_i32_e32 v91, 31, v90
	v_ashrrev_i32_e32 v83, 31, v82
	v_ashrrev_i32_e32 v75, 31, v74
	v_ashrrev_i32_e32 v59, 31, v58
	v_cvt_pk_fp8_f32 v65, v62, v63 op_sel:[0,0,1]
	v_pk_add_f32 v[52:53], v[52:53], v[136:137]
	v_cvt_pk_fp8_f32 v35, v28, v29 op_sel:[0,0,1]
	v_pk_add_f32 v[20:21], v[20:21], v[136:137]
	v_lshl_add_u32 v160, v151, 4, s18
	v_lshlrev_b64 v[122:123], 11, v[124:125]
	v_lshlrev_b64 v[114:115], 11, v[114:115]
	v_lshlrev_b64 v[106:107], 11, v[106:107]
	v_lshlrev_b64 v[98:99], 11, v[98:99]
	v_lshlrev_b64 v[90:91], 11, v[90:91]
	v_lshlrev_b64 v[82:83], 11, v[82:83]
	v_lshlrev_b64 v[74:75], 11, v[74:75]
	v_lshlrev_b64 v[58:59], 11, v[58:59]
	v_cvt_pk_fp8_f32 v61, v52, v53 op_sel:[0,0,1]
	v_pk_add_f32 v[44:45], v[44:45], v[136:137]
	v_cvt_pk_fp8_f32 v27, v20, v21 op_sel:[0,0,1]
	v_pk_add_f32 v[12:13], v[12:13], v[136:137]
	v_ashrrev_i32_e32 v161, 31, v160
	v_lshl_add_u64 v[122:123], s[4:5], 0, v[122:123]
	v_lshl_add_u64 v[114:115], s[4:5], 0, v[114:115]
	v_lshl_add_u64 v[106:107], s[4:5], 0, v[106:107]
	v_lshl_add_u64 v[98:99], s[4:5], 0, v[98:99]
	v_lshl_add_u64 v[90:91], s[4:5], 0, v[90:91]
	v_lshl_add_u64 v[82:83], s[4:5], 0, v[82:83]
	v_lshl_add_u64 v[74:75], s[4:5], 0, v[74:75]
	v_lshl_add_u64 v[58:59], s[4:5], 0, v[58:59]
	v_cvt_pk_fp8_f32 v51, v44, v45 op_sel:[0,0,1]
	v_pk_add_f32 v[36:37], v[36:37], v[136:137]
	v_cvt_pk_fp8_f32 v19, v12, v13 op_sel:[0,0,1]
	v_pk_add_f32 v[2:3], v[8:9], v[132:133]
	v_pk_add_f32 v[4:5], v[4:5], v[136:137]
	v_lshl_add_u64 v[122:123], v[122:123], 0, v[160:161]
	v_lshl_add_u64 v[114:115], v[114:115], 0, v[160:161]
	v_lshl_add_u64 v[106:107], v[106:107], 0, v[160:161]
	v_lshl_add_u64 v[98:99], v[98:99], 0, v[160:161]
	v_lshl_add_u64 v[90:91], v[90:91], 0, v[160:161]
	v_lshl_add_u64 v[82:83], v[82:83], 0, v[160:161]
	v_lshl_add_u64 v[74:75], v[74:75], 0, v[160:161]
	v_lshl_add_u64 v[58:59], v[58:59], 0, v[160:161]
	v_cvt_pk_fp8_f32 v43, v36, v37 op_sel:[0,0,1]
	v_cvt_pk_fp8_f32 v10, v2, v3 op_sel:[0,0,1]
	v_cvt_pk_fp8_f32 v11, v4, v5 op_sel:[0,0,1]
	s_andn2_b64 vcc, exec, s[16:17]
	s_mov_b64 s[16:17], -1
	v_mov_b32_e32 v244, v162
	v_mov_b32_e32 v245, v163
	v_mov_b32_e32 v246, v64
	v_mov_b32_e32 v247, v65
	global_store_dwordx4 v[122:123], v[244:247], off nt
	v_mov_b32_e32 v248, v126
	v_mov_b32_e32 v249, v127
	v_mov_b32_e32 v250, v60
	v_mov_b32_e32 v251, v61
	global_store_dwordx4 v[114:115], v[248:251], off nt
	v_mov_b32_e32 v244, v116
	v_mov_b32_e32 v245, v117
	v_mov_b32_e32 v246, v50
	v_mov_b32_e32 v247, v51
	global_store_dwordx4 v[106:107], v[244:247], off nt
	v_mov_b32_e32 v248, v108
	v_mov_b32_e32 v249, v109
	v_mov_b32_e32 v250, v42
	v_mov_b32_e32 v251, v43
	global_store_dwordx4 v[98:99], v[248:251], off nt
	v_mov_b32_e32 v244, v100
	v_mov_b32_e32 v245, v101
	v_mov_b32_e32 v246, v34
	v_mov_b32_e32 v247, v35
	global_store_dwordx4 v[90:91], v[244:247], off nt
	v_mov_b32_e32 v248, v92
	v_mov_b32_e32 v249, v93
	v_mov_b32_e32 v250, v26
	v_mov_b32_e32 v251, v27
	global_store_dwordx4 v[82:83], v[248:251], off nt
	v_mov_b32_e32 v244, v84
	v_mov_b32_e32 v245, v85
	v_mov_b32_e32 v246, v18
	v_mov_b32_e32 v247, v19
	global_store_dwordx4 v[74:75], v[244:247], off nt
	v_mov_b32_e32 v248, v76
	v_mov_b32_e32 v249, v77
	v_mov_b32_e32 v250, v10
	v_mov_b32_e32 v251, v11
	global_store_dwordx4 v[58:59], v[248:251], off nt
	s_cbranch_vccnz .LBB5_1672
	v_readfirstlane_b32 s11, v0
	s_cmpk_gt_u32 s11, 0xff
	s_cbranch_scc1 .LBB5_1684
	v_readlane_b32 s56, v253, 2
	s_and_b32 s18, s11, 0xc0
	s_ashr_i32 s11, s10, 31
	v_readlane_b32 s57, v253, 3
	v_readlane_b32 s58, v253, 4
	v_readlane_b32 s59, v253, 5
	v_readlane_b32 s60, v253, 6
	v_readlane_b32 s61, v253, 7
	s_lshl_b64 s[16:17], s[10:11], 13
	v_readlane_b32 s62, v253, 8
	v_readlane_b32 s63, v253, 9
	s_mov_b64 s[56:57], s[60:61]
	s_add_u32 s11, s56, s16
	s_addc_u32 s19, s57, s17
	s_lshl_b32 s16, s52, 8
	s_ashr_i32 s17, s16, 31
	s_lshl_b64 s[16:17], s[16:17], 2
	s_add_u32 s16, s11, s16
	s_addc_u32 s17, s19, s17
	s_lshl_b32 s11, s55, 11
	s_and_b32 s11, s11, 0x800
	s_add_i32 s11, s11, 0
	s_lshl_b32 s18, s18, 2
	s_add_i32 s11, s11, s18
	s_add_i32 m0, s11, 0x20c00
	s_mov_b64 s[58:59], s[62:63]
	global_load_lds_dword v150, s[16:17]
